# P3 scan software-pipelined: next 16-chunk group's loads issued into a second register set before the current group is processed
# speedup vs baseline: 1.0018x; 1.0018x over previous
; __device__ __forceinline__ void p3_scan(Ctx& X) {
;     ...
;     for (int item = gt; item < 65536 + 32768; item += NGT) {
;         const bool ret = item < 65536; const int it2 = ret ? item : item - 65536;
;         bf16* p = ret ? (XP_KV(X) + (size_t)it2 * 4) : (XP_SST(X) + (size_t)it2 * 4);
;         const size_t stride = ret ? 262144 : 131072;
;         const int head = ret ? (it2 >> 14) : (it2 >> 11);
;         const float gdec = ret ? GAMMA_CHUNK[head & 3] : 0.f;
;         float s0 = 0.f, s1 = 0.f, s2 = 0.f, s3 = 0.f;
;         for (int c0 = 0; c0 < NCHUNK; c0 += 16) {
;             u32x2 v[16]; float dec[16];
; #pragma unroll
;             for (int j = 0; j < 16; ++j) { v[j] = *(const u32x2*)(p + (size_t)(c0 + j) * stride); dec[j] = ret ? gdec : XP_ADEC(X)[(c0 + j) * 16 + head]; }
.LBB0_441:
.LBB0_442:
	v_mov_b32_e32 v212, v6
	v_mov_b64_e32 v[210:211], v[8:9]
	global_load_dwordx2 v[136:137], v[210:211], off
	s_waitcnt vmcnt(1)
	v_mov_b32_e32 v208, v3
	s_and_saveexec_b64 s[2:3], vcc
	s_cbranch_execz .Lsca_444
	v_ashrrev_i32_e32 v213, 31, v212
	v_lshl_add_u64 v[124:125], v[212:213], 2, s[8:9]
	global_load_dword v208, v[124:125], off
.Lsca_444:
	s_or_b64 exec, exec, s[2:3]
	v_lshl_add_u64 v[162:163], v[210:211], 0, v[38:39]
	global_load_dwordx2 v[140:141], v[162:163], off
	v_mov_b32_e32 v127, v3
	s_and_saveexec_b64 s[2:3], vcc
	s_cbranch_execz .Lsca_446
	v_add_u32_e32 v124, 16, v212
	v_ashrrev_i32_e32 v125, 31, v124
	v_lshl_add_u64 v[124:125], v[124:125], 2, s[8:9]
	global_load_dword v127, v[124:125], off
.Lsca_446:
	s_or_b64 exec, exec, s[2:3]
	v_lshl_add_u64 v[168:169], v[210:211], 0, v[36:37]
	global_load_dwordx2 v[142:143], v[168:169], off
	v_mov_b32_e32 v133, v3
	s_and_saveexec_b64 s[2:3], vcc
	s_cbranch_execz .Lsca_448
	v_add_u32_e32 v124, 32, v212
	v_ashrrev_i32_e32 v125, 31, v124
	v_lshl_add_u64 v[124:125], v[124:125], 2, s[8:9]
	global_load_dword v133, v[124:125], off
.Lsca_448:
	s_or_b64 exec, exec, s[2:3]
	v_lshl_add_u64 v[174:175], v[210:211], 0, v[34:35]
	global_load_dwordx2 v[148:149], v[174:175], off
	v_mov_b32_e32 v145, v3
	s_and_saveexec_b64 s[2:3], vcc
	s_cbranch_execz .Lsca_450
	v_add_u32_e32 v124, 48, v212
	v_ashrrev_i32_e32 v125, 31, v124
	v_lshl_add_u64 v[124:125], v[124:125], 2, s[8:9]
	global_load_dword v145, v[124:125], off
.Lsca_450:
	s_or_b64 exec, exec, s[2:3]
	v_lshl_add_u64 v[178:179], v[210:211], 0, v[32:33]
	global_load_dwordx2 v[152:153], v[178:179], off
	v_mov_b32_e32 v155, v3
	s_and_saveexec_b64 s[2:3], vcc
	s_cbranch_execz .Lsca_452
	v_add_u32_e32 v124, 64, v212
	v_ashrrev_i32_e32 v125, 31, v124
	v_lshl_add_u64 v[124:125], v[124:125], 2, s[8:9]
	global_load_dword v155, v[124:125], off
.Lsca_452:
	s_or_b64 exec, exec, s[2:3]
	v_lshl_add_u64 v[182:183], v[210:211], 0, v[30:31]
	global_load_dwordx2 v[156:157], v[182:183], off
	v_mov_b32_e32 v173, v3
	s_and_saveexec_b64 s[2:3], vcc
	s_cbranch_execz .Lsca_454
	v_add_u32_e32 v124, 0x50, v212
	v_ashrrev_i32_e32 v125, 31, v124
	v_lshl_add_u64 v[124:125], v[124:125], 2, s[8:9]
	global_load_dword v173, v[124:125], off
.Lsca_454:
	s_or_b64 exec, exec, s[2:3]
	v_lshl_add_u64 v[184:185], v[210:211], 0, v[28:29]
	global_load_dwordx2 v[166:167], v[184:185], off
	v_mov_b32_e32 v200, v3
	s_and_saveexec_b64 s[2:3], vcc
	s_cbranch_execz .Lsca_456
	v_add_u32_e32 v124, 0x60, v212
	v_ashrrev_i32_e32 v125, 31, v124
	v_lshl_add_u64 v[124:125], v[124:125], 2, s[8:9]
	global_load_dword v200, v[124:125], off
.Lsca_456:
	s_or_b64 exec, exec, s[2:3]
	v_lshl_add_u64 v[188:189], v[210:211], 0, v[26:27]
	global_load_dwordx2 v[170:171], v[188:189], off
	v_mov_b32_e32 v201, v3
	s_and_saveexec_b64 s[2:3], vcc
	s_cbranch_execz .Lsca_458
	v_add_u32_e32 v124, 0x70, v212
	v_ashrrev_i32_e32 v125, 31, v124
	v_lshl_add_u64 v[124:125], v[124:125], 2, s[8:9]
	global_load_dword v201, v[124:125], off
.Lsca_458:
	s_or_b64 exec, exec, s[2:3]
	v_lshl_add_u64 v[190:191], v[210:211], 0, v[24:25]
	global_load_dwordx2 v[176:177], v[190:191], off
	v_mov_b32_e32 v202, v3
	s_and_saveexec_b64 s[2:3], vcc
	s_cbranch_execz .Lsca_460
	v_add_u32_e32 v124, 0x80, v212
	v_ashrrev_i32_e32 v125, 31, v124
	v_lshl_add_u64 v[124:125], v[124:125], 2, s[8:9]
	global_load_dword v202, v[124:125], off
.Lsca_460:
	s_or_b64 exec, exec, s[2:3]
	v_lshl_add_u64 v[192:193], v[210:211], 0, v[22:23]
	global_load_dwordx2 v[180:181], v[192:193], off
	v_mov_b32_e32 v203, v3
	s_and_saveexec_b64 s[2:3], vcc
	s_cbranch_execz .Lsca_462
	v_add_u32_e32 v124, 0x90, v212
	v_ashrrev_i32_e32 v125, 31, v124
	v_lshl_add_u64 v[124:125], v[124:125], 2, s[8:9]
	global_load_dword v203, v[124:125], off
.Lsca_462:
	s_or_b64 exec, exec, s[2:3]
	v_lshl_add_u64 v[196:197], v[210:211], 0, v[20:21]
	global_load_dwordx2 v[186:187], v[196:197], off
	v_mov_b32_e32 v204, v3
	s_and_saveexec_b64 s[2:3], vcc
	s_cbranch_execz .Lsca_464
	v_add_u32_e32 v124, 0xa0, v212
	v_ashrrev_i32_e32 v125, 31, v124
	v_lshl_add_u64 v[124:125], v[124:125], 2, s[8:9]
	global_load_dword v204, v[124:125], off
; __device__ __forceinline__ void p3_scan(Ctx& X) {
;     ...
;     for (int item = gt; item < 65536 + 32768; item += NGT) {
;         const bool ret = item < 65536; const int it2 = ret ? item : item - 65536;
;         bf16* p = ret ? (XP_KV(X) + (size_t)it2 * 4) : (XP_SST(X) + (size_t)it2 * 4);
;         const size_t stride = ret ? 262144 : 131072;
;         const int head = ret ? (it2 >> 14) : (it2 >> 11);
;         const float gdec = ret ? GAMMA_CHUNK[head & 3] : 0.f;
;         float s0 = 0.f, s1 = 0.f, s2 = 0.f, s3 = 0.f;
;         for (int c0 = 0; c0 < NCHUNK; c0 += 16) {
;             u32x2 v[16]; float dec[16];
; #pragma unroll
;             for (int j = 0; j < 16; ++j) { v[j] = *(const u32x2*)(p + (size_t)(c0 + j) * stride); dec[j] = ret ? gdec : XP_ADEC(X)[(c0 + j) * 16 + head]; }
.Lsca_464:
	s_or_b64 exec, exec, s[2:3]
	v_lshl_add_u64 v[124:125], v[210:211], 0, v[18:19]
	global_load_dwordx2 v[198:199], v[124:125], off
	v_mov_b32_e32 v126, v3
	s_and_saveexec_b64 s[2:3], vcc
	s_cbranch_execz .Lsca_466
	v_add_u32_e32 v128, 0xb0, v212
	v_ashrrev_i32_e32 v129, 31, v128
	v_lshl_add_u64 v[128:129], v[128:129], 2, s[8:9]
	global_load_dword v126, v[128:129], off
.Lsca_466:
	s_or_b64 exec, exec, s[2:3]
	v_lshl_add_u64 v[130:131], v[210:211], 0, v[16:17]
	global_load_dwordx2 v[128:129], v[130:131], off
	v_mov_b32_e32 v132, v3
	s_and_saveexec_b64 s[2:3], vcc
	s_cbranch_execz .Lsca_468
	v_add_u32_e32 v134, 0xc0, v212
	v_ashrrev_i32_e32 v135, 31, v134
	v_lshl_add_u64 v[134:135], v[134:135], 2, s[8:9]
	global_load_dword v132, v[134:135], off
.Lsca_468:
	s_or_b64 exec, exec, s[2:3]
	v_lshl_add_u64 v[138:139], v[210:211], 0, v[14:15]
	global_load_dwordx2 v[134:135], v[138:139], off
	v_mov_b32_e32 v144, v3
	s_and_saveexec_b64 s[2:3], vcc
	s_cbranch_execz .Lsca_470
	v_add_u32_e32 v146, 0xd0, v212
	v_ashrrev_i32_e32 v147, 31, v146
	v_lshl_add_u64 v[146:147], v[146:147], 2, s[8:9]
	global_load_dword v144, v[146:147], off
.Lsca_470:
	s_or_b64 exec, exec, s[2:3]
	v_lshl_add_u64 v[150:151], v[210:211], 0, v[12:13]
	global_load_dwordx2 v[146:147], v[150:151], off
	v_mov_b32_e32 v154, v3
	s_and_saveexec_b64 s[2:3], vcc
	s_cbranch_execz .Lsca_472
	v_add_u32_e32 v160, 0xe0, v212
	v_ashrrev_i32_e32 v161, 31, v160
	v_lshl_add_u64 v[160:161], v[160:161], 2, s[8:9]
	global_load_dword v154, v[160:161], off
.Lsca_472:
	s_or_b64 exec, exec, s[2:3]
	v_lshl_add_u64 v[164:165], v[210:211], 0, v[10:11]
	global_load_dwordx2 v[160:161], v[164:165], off
	v_mov_b32_e32 v172, v3
	s_and_saveexec_b64 s[2:3], vcc
	s_cbranch_execz .Lsca_end
	v_add_u32_e32 v206, 0xf0, v212
	v_ashrrev_i32_e32 v207, 31, v206
	v_lshl_add_u64 v[206:207], v[206:207], 2, s[8:9]
	global_load_dword v172, v[206:207], off
.Lsca_end:
	s_or_b64 exec, exec, s[2:3]
	s_waitcnt vmcnt(0)
.Lsc_top:
	v_mov_b64_e32 v[44:45], v[124:125]
	v_mov_b64_e32 v[46:47], v[126:127]
	v_mov_b64_e32 v[48:49], v[128:129]
	v_mov_b64_e32 v[50:51], v[130:131]
	v_mov_b64_e32 v[52:53], v[132:133]
	v_mov_b64_e32 v[54:55], v[134:135]
	v_mov_b64_e32 v[56:57], v[136:137]
	v_mov_b64_e32 v[58:59], v[138:139]
	v_mov_b64_e32 v[60:61], v[140:141]
	v_mov_b64_e32 v[62:63], v[142:143]
	v_mov_b64_e32 v[64:65], v[144:145]
	v_mov_b64_e32 v[66:67], v[146:147]
	v_mov_b64_e32 v[68:69], v[148:149]
	v_mov_b64_e32 v[70:71], v[150:151]
	v_mov_b64_e32 v[72:73], v[152:153]
	v_mov_b64_e32 v[74:75], v[154:155]
	v_mov_b64_e32 v[76:77], v[156:157]
	v_mov_b64_e32 v[78:79], v[160:161]
	v_mov_b64_e32 v[80:81], v[162:163]
	v_mov_b64_e32 v[82:83], v[164:165]
	v_mov_b64_e32 v[84:85], v[166:167]
	v_mov_b64_e32 v[86:87], v[168:169]
	v_mov_b64_e32 v[88:89], v[170:171]
	v_mov_b64_e32 v[90:91], v[172:173]
	v_mov_b64_e32 v[92:93], v[174:175]
	v_mov_b64_e32 v[94:95], v[176:177]
	v_mov_b64_e32 v[96:97], v[178:179]
	v_mov_b64_e32 v[98:99], v[180:181]
	v_mov_b64_e32 v[100:101], v[182:183]
	v_mov_b64_e32 v[102:103], v[184:185]
	v_mov_b64_e32 v[104:105], v[186:187]
	v_mov_b64_e32 v[106:107], v[188:189]
	v_mov_b64_e32 v[108:109], v[190:191]
	v_mov_b64_e32 v[110:111], v[192:193]
	v_mov_b64_e32 v[112:113], v[196:197]
	v_mov_b64_e32 v[114:115], v[198:199]
	v_mov_b64_e32 v[116:117], v[200:201]
	v_mov_b64_e32 v[118:119], v[202:203]
	v_mov_b64_e32 v[120:121], v[204:205]
	v_mov_b64_e32 v[122:123], v[206:207]
	v_mov_b32_e32 v7, v208
	s_cmp_lt_i32 s12, 32
	s_cbranch_scc0 .Lsc_nopf
	v_lshl_add_u64 v[210:211], v[8:9], 0, v[4:5]
	v_add_u32_e32 v212, 0x100, v6
	global_load_dwordx2 v[136:137], v[210:211], off
	v_mov_b32_e32 v208, v3
	s_and_saveexec_b64 s[2:3], vcc
	s_cbranch_execz .Lscb_444
	v_ashrrev_i32_e32 v213, 31, v212
	v_lshl_add_u64 v[124:125], v[212:213], 2, s[8:9]
	global_load_dword v208, v[124:125], off

; __device__ __forceinline__ unsigned pk_bf16(float lo, float hi) { unsigned r; asm("v_cvt_pk_bf16_f32 %0, %1, %2" : "=v"(r) : "v"(lo), "v"(hi)); return r; }
; __device__ __forceinline__ float bf_lo(unsigned u) { return __uint_as_float(u << 16); }
; __device__ __forceinline__ float bf_hi(unsigned u) { return __uint_as_float(u & 0xffff0000u); }
; __device__ __forceinline__ void p3_scan(Ctx& X) {
;     ...
; #pragma unroll
;             for (int j = 0; j < 16; ++j) { u32x2 o; o.x = pk_bf16(s0, s1); o.y = pk_bf16(s2, s3); *(u32x2*)(p + (size_t)(c0 + j) * stride) = o;
;                 s0 = dec[j] * s0 + bf_lo(v[j].x); s1 = dec[j] * s1 + bf_hi(v[j].x); s2 = dec[j] * s2 + bf_lo(v[j].y); s3 = dec[j] * s3 + bf_hi(v[j].y); }
;         }
.Lsc_nopf:
	v_lshlrev_b32_e32 v121, 16, v56
	v_cvt_pk_bf16_f32 v122, v43, v42
	v_fmac_f32_e32 v121, v43, v7
	v_and_b32_e32 v43, 0xffff0000, v56
	v_fmac_f32_e32 v43, v42, v7
	v_lshlrev_b32_e32 v42, 16, v57
	v_and_b32_e32 v56, 0xffff0000, v57
	v_and_b32_e32 v57, 0xffff0000, v60
	v_cvt_pk_bf16_f32 v123, v41, v40
	v_fmac_f32_e32 v42, v41, v7
	v_fmac_f32_e32 v56, v40, v7
	v_cvt_pk_bf16_f32 v40, v121, v43
	v_fmac_f32_e32 v57, v43, v47
	v_lshlrev_b32_e32 v43, 16, v61
	v_cvt_pk_bf16_f32 v41, v42, v56
	v_lshlrev_b32_e32 v7, 16, v60
	v_fmac_f32_e32 v43, v42, v47
	v_and_b32_e32 v42, 0xffff0000, v61
	v_fmac_f32_e32 v7, v121, v47
	v_fmac_f32_e32 v42, v56, v47
	v_lshlrev_b32_e32 v47, 16, v62
	v_lshlrev_b32_e32 v56, 16, v63
	global_store_dwordx2 v[8:9], v[122:123], off
	global_store_dwordx2 v[80:81], v[40:41], off
	v_cvt_pk_bf16_f32 v40, v7, v57
	v_cvt_pk_bf16_f32 v41, v43, v42
	v_fmac_f32_e32 v47, v7, v53
	v_and_b32_e32 v7, 0xffff0000, v62
	v_fmac_f32_e32 v56, v43, v53
	v_and_b32_e32 v43, 0xffff0000, v63
	v_fmac_f32_e32 v7, v57, v53
	v_fmac_f32_e32 v43, v42, v53
	v_lshlrev_b32_e32 v42, 16, v68
	v_and_b32_e32 v53, 0xffff0000, v69
	global_store_dwordx2 v[86:87], v[40:41], off
	v_cvt_pk_bf16_f32 v40, v47, v7
	v_cvt_pk_bf16_f32 v41, v56, v43
	v_fmac_f32_e32 v42, v47, v65
	v_and_b32_e32 v47, 0xffff0000, v68
	v_fmac_f32_e32 v53, v43, v65
	v_lshlrev_b32_e32 v43, 16, v72
	global_store_dwordx2 v[92:93], v[40:41], off
	v_fmac_f32_e32 v47, v7, v65
	v_lshlrev_b32_e32 v7, 16, v69
	v_cvt_pk_bf16_f32 v40, v42, v47
	v_fmac_f32_e32 v43, v42, v75
	v_and_b32_e32 v42, 0xffff0000, v72
	v_fmac_f32_e32 v7, v56, v65
	v_fmac_f32_e32 v42, v47, v75
	v_lshlrev_b32_e32 v47, 16, v73
	v_cvt_pk_bf16_f32 v41, v7, v53
	v_fmac_f32_e32 v47, v7, v75
	v_and_b32_e32 v7, 0xffff0000, v73
	v_fmac_f32_e32 v7, v53, v75
	v_lshlrev_b32_e32 v53, 16, v76
	global_store_dwordx2 v[96:97], v[40:41], off
	v_cvt_pk_bf16_f32 v40, v43, v42
	v_fmac_f32_e32 v53, v43, v91
	v_and_b32_e32 v43, 0xffff0000, v76
	v_fmac_f32_e32 v43, v42, v91
	v_lshlrev_b32_e32 v42, 16, v77
	v_cvt_pk_bf16_f32 v41, v47, v7
	v_fmac_f32_e32 v42, v47, v91
	v_and_b32_e32 v47, 0xffff0000, v77
	v_fmac_f32_e32 v47, v7, v91
	v_lshlrev_b32_e32 v7, 16, v84
	global_store_dwordx2 v[100:101], v[40:41], off
	v_cvt_pk_bf16_f32 v40, v53, v43
	v_fmac_f32_e32 v7, v53, v116
	v_and_b32_e32 v53, 0xffff0000, v84
	v_fmac_f32_e32 v53, v43, v116
	v_lshlrev_b32_e32 v43, 16, v85
	v_cvt_pk_bf16_f32 v41, v42, v47
	v_fmac_f32_e32 v43, v42, v116
	v_and_b32_e32 v42, 0xffff0000, v85
	v_fmac_f32_e32 v42, v47, v116
	v_lshlrev_b32_e32 v47, 16, v88
	global_store_dwordx2 v[102:103], v[40:41], off
	v_cvt_pk_bf16_f32 v40, v7, v53
	v_fmac_f32_e32 v47, v7, v117
	v_and_b32_e32 v7, 0xffff0000, v88
	v_fmac_f32_e32 v7, v53, v117
	v_lshlrev_b32_e32 v53, 16, v89
	v_cvt_pk_bf16_f32 v41, v43, v42
	v_fmac_f32_e32 v53, v43, v117
	v_and_b32_e32 v43, 0xffff0000, v89
	v_fmac_f32_e32 v43, v42, v117
	v_lshlrev_b32_e32 v42, 16, v94
	global_store_dwordx2 v[106:107], v[40:41], off
	v_cvt_pk_bf16_f32 v40, v47, v7
	v_fmac_f32_e32 v42, v47, v118
	v_and_b32_e32 v47, 0xffff0000, v94
	v_fmac_f32_e32 v47, v7, v118
	v_lshlrev_b32_e32 v7, 16, v95
	v_cvt_pk_bf16_f32 v41, v53, v43
	v_fmac_f32_e32 v7, v53, v118
	v_and_b32_e32 v53, 0xffff0000, v95
	v_fmac_f32_e32 v53, v43, v118
	v_lshlrev_b32_e32 v43, 16, v98
	global_store_dwordx2 v[108:109], v[40:41], off
	v_cvt_pk_bf16_f32 v40, v42, v47
	v_fmac_f32_e32 v43, v42, v119
	v_and_b32_e32 v42, 0xffff0000, v98
	v_fmac_f32_e32 v42, v47, v119
	v_lshlrev_b32_e32 v47, 16, v99
	v_cvt_pk_bf16_f32 v41, v7, v53
	v_fmac_f32_e32 v47, v7, v119
	v_and_b32_e32 v7, 0xffff0000, v99
	global_store_dwordx2 v[110:111], v[40:41], off
	v_fmac_f32_e32 v7, v53, v119
	v_cvt_pk_bf16_f32 v40, v43, v42
	v_cvt_pk_bf16_f32 v41, v47, v7
	global_store_dwordx2 v[112:113], v[40:41], off
	v_mul_f32_e32 v41, v43, v120
	v_lshlrev_b32_e32 v43, 16, v104
	v_mul_f32_e32 v40, v42, v120
	v_and_b32_e32 v42, 0xffff0000, v104
	v_mul_f32_e32 v57, v47, v120
	v_lshlrev_b32_e32 v61, 16, v105
	v_mul_f32_e32 v56, v7, v120
	v_and_b32_e32 v60, 0xffff0000, v105
	v_lshlrev_b32_e32 v63, 16, v114
	v_and_b32_e32 v62, 0xffff0000, v114
	v_pk_add_f32 v[40:41], v[40:41], v[42:43]
	v_lshlrev_b32_e32 v69, 16, v115
	v_and_b32_e32 v68, 0xffff0000, v115
	v_cvt_pk_bf16_f32 v72, v41, v40
	v_pk_fma_f32 v[40:41], v[40:41], v[46:47], v[62:63] op_sel_hi:[1,0,1]
	v_and_b32_e32 v42, 0xffff0000, v48
	v_lshlrev_b32_e32 v43, 16, v48
	v_pk_add_f32 v[56:57], v[56:57], v[60:61]
	v_pk_fma_f32 v[62:63], v[40:41], v[52:53], v[42:43] op_sel_hi:[1,0,1]
	v_cvt_pk_bf16_f32 v73, v57, v56
	global_store_dwordx2 v[44:45], v[72:73], off
	v_pk_fma_f32 v[44:45], v[56:57], v[46:47], v[68:69] op_sel_hi:[1,0,1]
	v_cvt_pk_bf16_f32 v40, v41, v40
	v_and_b32_e32 v42, 0xffff0000, v54
	v_cvt_pk_bf16_f32 v41, v45, v44
	global_store_dwordx2 v[50:51], v[40:41], off
	v_and_b32_e32 v40, 0xffff0000, v49
	v_lshlrev_b32_e32 v41, 16, v49
	v_pk_fma_f32 v[40:41], v[44:45], v[52:53], v[40:41] op_sel_hi:[1,0,1]
	v_cvt_pk_bf16_f32 v44, v63, v62
	v_lshlrev_b32_e32 v43, 16, v54
	v_cvt_pk_bf16_f32 v45, v41, v40
	global_store_dwordx2 v[58:59], v[44:45], off
	v_and_b32_e32 v44, 0xffff0000, v55
	v_lshlrev_b32_e32 v45, 16, v55
	v_pk_fma_f32 v[76:77], v[62:63], v[64:65], v[42:43] op_sel_hi:[1,0,1]
	v_pk_fma_f32 v[40:41], v[40:41], v[64:65], v[44:45] op_sel_hi:[1,0,1]
	v_cvt_pk_bf16_f32 v44, v77, v76
	v_and_b32_e32 v42, 0xffff0000, v66
	v_cvt_pk_bf16_f32 v45, v41, v40
	v_lshlrev_b32_e32 v43, 16, v66
	global_store_dwordx2 v[70:71], v[44:45], off
	v_and_b32_e32 v44, 0xffff0000, v67
	v_lshlrev_b32_e32 v45, 16, v67
	v_pk_fma_f32 v[80:81], v[76:77], v[74:75], v[42:43] op_sel_hi:[1,0,1]
	v_pk_fma_f32 v[40:41], v[40:41], v[74:75], v[44:45] op_sel_hi:[1,0,1]
	v_cvt_pk_bf16_f32 v44, v81, v80
	v_and_b32_e32 v42, 0xffff0000, v78
	v_cvt_pk_bf16_f32 v45, v41, v40
	v_lshlrev_b32_e32 v43, 16, v78
	global_store_dwordx2 v[82:83], v[44:45], off
	v_and_b32_e32 v44, 0xffff0000, v79
	v_lshlrev_b32_e32 v45, 16, v79
	s_add_i32 s12, s12, 16
	v_pk_fma_f32 v[42:43], v[80:81], v[90:91], v[42:43] op_sel_hi:[1,0,1]
	v_pk_fma_f32 v[40:41], v[40:41], v[90:91], v[44:45] op_sel_hi:[1,0,1]
	v_add_u32_e32 v6, 0x100, v6
	s_cmp_gt_u32 s12, 47
	v_lshl_add_u64 v[8:9], v[8:9], 0, v[4:5]
	s_cbranch_scc1 .LBB0_433
	s_waitcnt vmcnt(16)
	s_branch .Lsc_top
